# static s_setprio 1 for waves 4-7 across the attention mainloop (strategy 4: younger-half priority raise)
# speedup vs baseline: 1.0052x; 1.0052x over previous
; template <int CTRL> __device__ __forceinline__ float dpp_f(float v) { return __uint_as_float((unsigned)__builtin_amdgcn_update_dpp(0, (int)__float_as_uint(v), CTRL, 0xF, 0xF, true)); }
; __device__ __forceinline__ float swap16_max(float a) { const auto r = __builtin_amdgcn_permlane16_swap(__float_as_uint(a), __float_as_uint(a), false, false); return fmaxf(__uint_as_float(r[0]), __uint_as_float(r[1])); }
; __device__ __forceinline__ float swap32_max(float a) { const auto r = __builtin_amdgcn_permlane32_swap(__float_as_uint(a), __float_as_uint(a), false, false); return fmaxf(__uint_as_float(r[0]), __uint_as_float(r[1])); }
; __global__ void __launch_bounds__(NTHR, 2) fwd_kernel(Args args) {
;     ...
;             __syncthreads();
;             float gq_ = fabsf(INP(F, I_QNORM)[l * 64 + F.lane]), gk_ = fabsf(INP(F, I_KNORM)[l * 64 + F.lane]);
;             gq_ = fmaxf(gq_, dpp_f<DPP_X1>(gq_)); gq_ = fmaxf(gq_, dpp_f<DPP_X2>(gq_)); gq_ = fmaxf(gq_, dpp_f<DPP_HMIR>(gq_)); gq_ = fmaxf(gq_, dpp_f<DPP_MIR>(gq_)); gq_ = swap16_max(gq_); gq_ = swap32_max(gq_);
;             gk_ = fmaxf(gk_, dpp_f<DPP_X1>(gk_)); gk_ = fmaxf(gk_, dpp_f<DPP_X2>(gk_)); gk_ = fmaxf(gk_, dpp_f<DPP_HMIR>(gk_)); gk_ = fmaxf(gk_, dpp_f<DPP_MIR>(gk_)); gk_ = swap16_max(gk_); gk_ = swap32_max(gk_);
;             const float mfix = __uint_as_float(__builtin_amdgcn_readfirstlane(__float_as_uint(1.02f * ATT_C2 * 64.0f * gq_ * gk_)));
;             const bool nomax = mfix <= 60.0f;
;             REPS(13) for (int i = 0; ; ++i) { const int U = split ? F.vcu + F.G * i : 2 * F.vcu + i; if (U >= 512 || (!split && i >= 2)) break;
;                     const int grp = U >> 6, j = U & 63, b = grp >> 1, h = (grp & 1) * 4 + (j >> 4), qb = j & 15;
;                     if (nomax) attn_body::attn_unit<8, true>(b, h, qb, (const attn_body::bf16*)(F.ws + WS_QP), (const attn_body::bf16*)(F.ws + WS_KV), (const attn_body::bf16*)(F.ws + WS_KV) + 128,
;                                             (attn_body::bf16*)(F.ws + WS_CAT) + 256, (char*)lds, mfix);
;                     else attn_body::attn_unit<8>(b, h, qb, (const attn_body::bf16*)(F.ws + WS_QP), (const attn_body::bf16*)(F.ws + WS_KV), (const attn_body::bf16*)(F.ws + WS_KV) + 128,
;                                             (attn_body::bf16*)(F.ws + WS_CAT) + 256, (char*)lds); }
.LBB0_711:
	v_readlane_b32 s2, v254, 36
	s_barrier
	s_nop 0
	v_mov_b32_e32 v1, s2
	s_barrier
	ds_read_b128 v[2:5], v1
	v_readlane_b32 s4, v255, 5
	s_andn2_b64 vcc, exec, s[10:11]
	s_mov_b64 s[46:47], 0x20000
	v_lshl_or_b32 v182, s4, 6, v186
	s_waitcnt lgkmcnt(0)
	v_readfirstlane_b32 s2, v2
	v_readfirstlane_b32 s3, v3
	v_lshlrev_b64 v[2:3], 2, v[182:183]
	s_waitcnt vmcnt(0)
	v_lshl_add_u64 v[6:7], s[2:3], 0, v[2:3]
	v_readfirstlane_b32 s2, v4
	v_readfirstlane_b32 s3, v5
	global_load_dword v1, v[6:7], off
	s_nop 0
	v_lshl_add_u64 v[2:3], s[2:3], 0, v[2:3]
	global_load_dword v2, v[2:3], off
	s_waitcnt vmcnt(0)
	v_and_b32_e32 v3, 0x7fffffff, v1
	s_nop 1
	v_mov_b32_dpp v3, v3 quad_perm:[1,0,3,2] row_mask:0xf bank_mask:0xf bound_ctrl:1
	v_max_f32_e64 v1, |v1|, |v1|
	v_and_b32_e32 v4, 0x7fffffff, v2
	v_max_f32_e32 v3, v3, v3
	v_max_f32_e64 v2, |v2|, |v2|
	v_mov_b32_dpp v4, v4 quad_perm:[1,0,3,2] row_mask:0xf bank_mask:0xf bound_ctrl:1
	v_max_f32_e32 v4, v4, v4
	v_max_f32_e32 v1, v1, v3
	v_max_f32_e32 v2, v2, v4
	s_nop 0
	v_mov_b32_dpp v3, v1 quad_perm:[2,3,0,1] row_mask:0xf bank_mask:0xf bound_ctrl:1
	v_mov_b32_dpp v4, v2 quad_perm:[2,3,0,1] row_mask:0xf bank_mask:0xf bound_ctrl:1
	v_max_f32_e32 v3, v3, v3
	v_max_f32_e32 v4, v4, v4
	v_max_f32_e32 v1, v1, v3
	v_max_f32_e32 v2, v2, v4
	s_nop 0
	v_mov_b32_dpp v3, v1 row_half_mirror row_mask:0xf bank_mask:0xf bound_ctrl:1
	v_mov_b32_dpp v4, v2 row_half_mirror row_mask:0xf bank_mask:0xf bound_ctrl:1
	v_max_f32_e32 v3, v3, v3
	v_max_f32_e32 v4, v4, v4
	v_max_f32_e32 v1, v1, v3
	v_max_f32_e32 v2, v2, v4
	s_nop 0
	v_mov_b32_dpp v3, v1 row_mirror row_mask:0xf bank_mask:0xf bound_ctrl:1
	v_mov_b32_dpp v4, v2 row_mirror row_mask:0xf bank_mask:0xf bound_ctrl:1
	v_max_f32_e32 v3, v3, v3
	v_max_f32_e32 v4, v4, v4
	v_max_f32_e32 v1, v1, v3
	v_max_f32_e32 v2, v2, v4
	v_mov_b32_e32 v3, v1
	v_mov_b32_e32 v4, v2
	s_nop 0
	v_permlane16_swap_b32_e32 v1, v3
	v_permlane16_swap_b32_e32 v2, v4
	v_max_f32_e32 v3, v3, v3
	v_max_f32_e32 v1, v1, v1
	v_max_f32_e32 v4, v4, v4
	v_max_f32_e32 v2, v2, v2
	v_max_f32_e32 v1, v1, v3
	v_max_f32_e32 v2, v2, v4
	v_mov_b32_e32 v3, v1
	v_mov_b32_e32 v4, v2
	s_nop 0
	v_permlane32_swap_b32_e32 v1, v3
	v_permlane32_swap_b32_e32 v2, v4
	v_max_f32_e32 v3, v3, v3
	v_max_f32_e32 v1, v1, v1
	v_max_f32_e32 v4, v4, v4
	v_max_f32_e32 v2, v2, v2
	v_max_f32_e32 v1, v1, v3
	v_max_f32_e32 v2, v2, v4
	v_mul_f32_e32 v1, 0x413c5bb7, v1
	v_mul_f32_e32 v1, v1, v2
	s_nop 0
	v_readfirstlane_b32 s34, v1
	s_cbranch_vccnz .LBB0_773
	s_lshl_b32 s3, s22, 1
	s_ashr_i32 s2, s22, 6
	s_or_b32 s35, s3, 1
	s_and_b32 s36, s3, 14
	s_ashr_i32 s3, s2, 31
	s_lshl_b64 s[8:9], s[2:3], 12
	s_lshl_b64 s[2:3], s[2:3], 21
	s_add_u32 s6, s58, s2
	s_addc_u32 s7, s59, s3
	s_lshl_b32 s10, s22, 2
	s_and_b32 s14, s10, 0x80
	s_add_u32 s6, s6, s14
	s_addc_u32 s7, s7, 0
	s_add_u32 s10, s6, 0xa400000
	s_addc_u32 s11, s7, 0
	s_add_u32 s12, s6, 0xa400100
	s_addc_u32 s13, s7, 0
	s_lshl_b32 s6, s22, 4
	s_and_b32 s6, s6, 0x380
	s_add_u32 s6, s58, s6
	s_addc_u32 s7, s59, 0
	s_add_u32 s37, s6, 0x9400000
	s_addc_u32 s38, s7, 0
	s_add_u32 s39, s6, 0xac00200
	s_addc_u32 s40, s7, 0
	s_or_b32 s2, s2, s14
	s_add_u32 s2, s58, s2
	s_addc_u32 s3, s59, s3
	s_add_u32 s14, s2, 0xa408000
	s_addc_u32 s15, s3, 0
	s_add_u32 s16, s2, 0xa408100
	s_addc_u32 s17, s3, 0
	v_mov_b32_e32 v1, 0x42700000
	s_add_u32 s18, s2, 0xa5d8000
	v_cmp_le_f32_e64 s[4:5], s34, v1
	s_addc_u32 s19, s3, 0
	s_mov_b32 s41, 0
	s_mov_b64 s[20:21], -1
	v_readfirstlane_b32 s93, v0
	s_nop 3
	s_lshr_b32 s93, s93, 6
	s_cmp_ge_u32 s93, 4
	s_cbranch_scc0 .Lattn_prio_done
	s_setprio 1
.Lattn_prio_done:
	s_branch .LBB0_715

; #define REPS(j) for (int rep_ = 0; rep_ < ((((REPMASK) >> (j)) & 1) ? 2 : 1); (++rep_, __syncthreads()))
; __global__ void __launch_bounds__(NTHR, 2) fwd_kernel(Args args) {
;     ...
;             REPS(13) for (int i = 0; ; ++i) { const int U = split ? F.vcu + F.G * i : 2 * F.vcu + i; if (U >= 512 || (!split && i >= 2)) break;
;                     const int grp = U >> 6, j = U & 63, b = grp >> 1, h = (grp & 1) * 4 + (j >> 4), qb = j & 15;
;                     if (nomax) attn_body::attn_unit<8, true>(b, h, qb, (const attn_body::bf16*)(F.ws + WS_QP), (const attn_body::bf16*)(F.ws + WS_KV), (const attn_body::bf16*)(F.ws + WS_KV) + 128,
;                                             (attn_body::bf16*)(F.ws + WS_CAT) + 256, (char*)lds, mfix);
;                     else attn_body::attn_unit<8>(b, h, qb, (const attn_body::bf16*)(F.ws + WS_QP), (const attn_body::bf16*)(F.ws + WS_KV), (const attn_body::bf16*)(F.ws + WS_KV) + 128,
;                                             (attn_body::bf16*)(F.ws + WS_CAT) + 256, (char*)lds); }
;             }
.LBB0_773:
	s_setprio 0
	v_readlane_b32 s54, v255, 5
	s_barrier
